# adds P0 silu fill and P7 gain fill: all loads in flight instead of one round trip per 512-element step
# speedup vs baseline: 1.0004x; 1.0004x over previous
; __device__ __forceinline__ float siluf(float x) { return x / (1.0f + __expf(-x)); }
; __device__ __forceinline__ void p0_mod(Frame& F, const Args& A) {
;     ...
;     if (F.vcu < 192) {
;         for (int k = F.tid; k < DM; k += 512) { sc[2 * k] = siluf(A.in[I_C][k]); sc[2 * k + 1] = siluf(A.in[I_C][2048 + k]); }
.LBB0_14:
	v_add_co_u32_e32 v6, vcc, 0x2000, v2
	s_nop 1
	v_addc_co_u32_e32 v7, vcc, 0, v3, vcc
	v_add_co_u32_e32 v20, vcc, 0x1000, v2
	s_nop 1
	v_addc_co_u32_e32 v21, vcc, 0, v3, vcc
	v_add_co_u32_e32 v22, vcc, 0x3000, v2
	s_nop 1
	v_addc_co_u32_e32 v23, vcc, 0, v3, vcc
	global_load_dword v24, v[2:3], off
	global_load_dword v25, v[6:7], off
	global_load_dword v26, v[2:3], off offset:2048
	global_load_dword v27, v[6:7], off offset:2048
	global_load_dword v28, v[20:21], off
	global_load_dword v29, v[22:23], off
	global_load_dword v30, v[20:21], off offset:2048
	global_load_dword v31, v[22:23], off offset:2048
	s_waitcnt vmcnt(6)
	v_mov_b32_e32 v8, v24
	v_mov_b32_e32 v9, v25
	v_mul_f32_e32 v6, 0xbfb8aa3b, v8
	v_exp_f32_e32 v6, v6
	v_mul_f32_e32 v7, 0xbfb8aa3b, v9
	v_exp_f32_e32 v7, v7
	s_nop 0
	v_pk_add_f32 v[6:7], v[6:7], 1.0 op_sel_hi:[1,0]
	s_nop 0
	v_div_scale_f32 v10, s[2:3], v7, v7, v9
	v_div_scale_f32 v12, s[2:3], v6, v6, v8
	v_rcp_f32_e32 v14, v10
	v_rcp_f32_e32 v15, v12
	v_div_scale_f32 v11, vcc, v9, v7, v9
	v_fma_f32 v16, -v10, v14, 1.0
	v_fma_f32 v17, -v12, v15, 1.0
	v_fmac_f32_e32 v14, v16, v14
	v_div_scale_f32 v13, s[4:5], v8, v6, v8
	v_fmac_f32_e32 v15, v17, v15
	v_mul_f32_e32 v16, v11, v14
	v_mul_f32_e32 v17, v13, v15
	v_fma_f32 v18, -v10, v16, v11
	v_fma_f32 v19, -v12, v17, v13
	v_fmac_f32_e32 v16, v18, v14
	v_fmac_f32_e32 v17, v19, v15
	v_fma_f32 v10, -v10, v16, v11
	v_fma_f32 v11, -v12, v17, v13
	v_div_fmas_f32 v10, v10, v14, v16
	s_mov_b64 vcc, s[4:5]
	v_div_fixup_f32 v7, v10, v7, v9
	v_div_fmas_f32 v9, v11, v15, v17
	v_div_fixup_f32 v6, v9, v6, v8
	ds_write_b64 v5, v[6:7]
	s_waitcnt vmcnt(4)
	v_mov_b32_e32 v8, v26
	v_mov_b32_e32 v9, v27
	v_mul_f32_e32 v6, 0xbfb8aa3b, v8
	v_exp_f32_e32 v6, v6
	v_mul_f32_e32 v7, 0xbfb8aa3b, v9
	v_exp_f32_e32 v7, v7
	s_nop 0
	v_pk_add_f32 v[6:7], v[6:7], 1.0 op_sel_hi:[1,0]
	s_nop 0
	v_div_scale_f32 v10, s[2:3], v7, v7, v9
	v_div_scale_f32 v12, s[2:3], v6, v6, v8
	v_rcp_f32_e32 v14, v10
	v_rcp_f32_e32 v15, v12
	v_div_scale_f32 v11, vcc, v9, v7, v9
	v_fma_f32 v16, -v10, v14, 1.0
	v_fma_f32 v17, -v12, v15, 1.0
	v_fmac_f32_e32 v14, v16, v14
	v_div_scale_f32 v13, s[4:5], v8, v6, v8
	v_fmac_f32_e32 v15, v17, v15
	v_mul_f32_e32 v16, v11, v14
	v_mul_f32_e32 v17, v13, v15
	v_fma_f32 v18, -v10, v16, v11
	v_fma_f32 v19, -v12, v17, v13
	v_fmac_f32_e32 v16, v18, v14
	v_fmac_f32_e32 v17, v19, v15
	v_fma_f32 v10, -v10, v16, v11
	v_fma_f32 v11, -v12, v17, v13
	v_div_fmas_f32 v10, v10, v14, v16
	s_mov_b64 vcc, s[4:5]
	v_div_fixup_f32 v7, v10, v7, v9
	v_div_fmas_f32 v9, v11, v15, v17
	v_div_fixup_f32 v6, v9, v6, v8
	ds_write_b64 v5, v[6:7] offset:4096
	s_waitcnt vmcnt(2)
	v_mov_b32_e32 v8, v28
	v_mov_b32_e32 v9, v29
	v_mul_f32_e32 v6, 0xbfb8aa3b, v8
	v_exp_f32_e32 v6, v6
	v_mul_f32_e32 v7, 0xbfb8aa3b, v9
	v_exp_f32_e32 v7, v7
	s_nop 0
	v_pk_add_f32 v[6:7], v[6:7], 1.0 op_sel_hi:[1,0]
	s_nop 0
	v_div_scale_f32 v10, s[2:3], v7, v7, v9
	v_div_scale_f32 v12, s[2:3], v6, v6, v8
	v_rcp_f32_e32 v14, v10
	v_rcp_f32_e32 v15, v12
	v_div_scale_f32 v11, vcc, v9, v7, v9
	v_fma_f32 v16, -v10, v14, 1.0
	v_fma_f32 v17, -v12, v15, 1.0
	v_fmac_f32_e32 v14, v16, v14
	v_div_scale_f32 v13, s[4:5], v8, v6, v8
	v_fmac_f32_e32 v15, v17, v15
	v_mul_f32_e32 v16, v11, v14
	v_mul_f32_e32 v17, v13, v15
	v_fma_f32 v18, -v10, v16, v11
	v_fma_f32 v19, -v12, v17, v13
	v_fmac_f32_e32 v16, v18, v14
	v_fmac_f32_e32 v17, v19, v15
	v_fma_f32 v10, -v10, v16, v11
	v_fma_f32 v11, -v12, v17, v13
	v_div_fmas_f32 v10, v10, v14, v16
	s_mov_b64 vcc, s[4:5]
	v_div_fixup_f32 v7, v10, v7, v9
	v_div_fmas_f32 v9, v11, v15, v17
	v_div_fixup_f32 v6, v9, v6, v8
	ds_write_b64 v5, v[6:7] offset:8192
	s_waitcnt vmcnt(0)
	v_mov_b32_e32 v8, v30
	v_mov_b32_e32 v9, v31
	v_mul_f32_e32 v6, 0xbfb8aa3b, v8
	v_exp_f32_e32 v6, v6
	v_mul_f32_e32 v7, 0xbfb8aa3b, v9
	v_exp_f32_e32 v7, v7
	s_nop 0
	v_pk_add_f32 v[6:7], v[6:7], 1.0 op_sel_hi:[1,0]
	s_nop 0
	v_div_scale_f32 v10, s[2:3], v7, v7, v9
	v_div_scale_f32 v12, s[2:3], v6, v6, v8
	v_rcp_f32_e32 v14, v10
	v_rcp_f32_e32 v15, v12
	v_div_scale_f32 v11, vcc, v9, v7, v9
	v_fma_f32 v16, -v10, v14, 1.0
	v_fma_f32 v17, -v12, v15, 1.0
	v_fmac_f32_e32 v14, v16, v14
	v_div_scale_f32 v13, s[4:5], v8, v6, v8
	v_fmac_f32_e32 v15, v17, v15
	v_mul_f32_e32 v16, v11, v14
	v_mul_f32_e32 v17, v13, v15
	v_fma_f32 v18, -v10, v16, v11
	v_fma_f32 v19, -v12, v17, v13
	v_fmac_f32_e32 v16, v18, v14
	v_fmac_f32_e32 v17, v19, v15
	v_fma_f32 v10, -v10, v16, v11
	v_fma_f32 v11, -v12, v17, v13
	v_div_fmas_f32 v10, v10, v14, v16
	s_mov_b64 vcc, s[4:5]
	v_div_fixup_f32 v7, v10, v7, v9
	v_div_fmas_f32 v9, v11, v15, v17
	v_div_fixup_f32 v6, v9, v6, v8
	ds_write_b64 v5, v[6:7] offset:12288
	s_or_b64 exec, exec, s[8:9]

; #define LAS __attribute__((address_space(3)))
; __device__ __forceinline__ void p7_router(Frame& F, const Args& A, bool commit = true) {
;     ...
;         for (int k = F.tid; k < DM; k += 512) { gainL[k] = A.in[I_N2G][k] * (1.0f + mod[4 * DM + k]); shiftL[k] = mod[3 * DM + k]; }
;         if (F.tid < 32) lcnt[F.tid] = 0;
;         __syncthreads();
;         {
;             const int i = F.lane & 31, kk = F.lane >> 5, kb = F.wave * 256 + kk * 128;
;             const float* hp = H1 + (size_t)(t0 + i) * DM + kb; const float* wp = A.in[I_WR] + (size_t)kb * 32 + i; const LAS float* gp = gainL + kb;
;             f32x16r acc = {}; float ss = 0.f;
; #pragma unroll 4
;             for (int s0 = 0; s0 < 128; s0 += 4) {
;                 const f32x4 hv = *(const f32x4*)(hp + s0); const f32x4 g4 = *(const LAS f32x4*)(gp + s0);
;                 const float b0 = wp[(s0 + 0) * 32], b1 = wp[(s0 + 1) * 32], b2 = wp[(s0 + 2) * 32], b3 = wp[(s0 + 3) * 32];
.LBB0_891:
	v_add_co_u32_e32 v242, vcc, 0xffffe000, v2
	s_nop 1
	v_addc_co_u32_e32 v243, vcc, -1, v3, vcc
	v_add_co_u32_e32 v244, vcc, 0x1000, v4
	s_nop 1
	v_addc_co_u32_e32 v245, vcc, 0, v5, vcc
	v_add_co_u32_e32 v248, vcc, 0x1000, v2
	s_nop 1
	v_addc_co_u32_e32 v249, vcc, 0, v3, vcc
	v_add_co_u32_e32 v250, vcc, 0x1000, v242
	s_nop 1
	v_addc_co_u32_e32 v251, vcc, 0, v243, vcc
	global_load_dword v230, v[4:5], off
	global_load_dword v231, v[2:3], off
	global_load_dword v232, v[242:243], off
	global_load_dword v233, v[4:5], off offset:2048
	global_load_dword v234, v[2:3], off offset:2048
	global_load_dword v235, v[242:243], off offset:2048
	global_load_dword v236, v[244:245], off
	global_load_dword v237, v[248:249], off
	global_load_dword v238, v[250:251], off
	global_load_dword v239, v[244:245], off offset:2048
	global_load_dword v240, v[248:249], off offset:2048
	global_load_dword v241, v[250:251], off offset:2048
	s_waitcnt vmcnt(9)
	v_add_f32_e32 v9, 1.0, v231
	v_mul_f32_e32 v9, v230, v9
	ds_write2st64_b32 v6, v9, v232 offset0:0 offset1:32
	s_waitcnt vmcnt(6)
	v_add_f32_e32 v10, 1.0, v234
	v_mul_f32_e32 v10, v233, v10
	ds_write2st64_b32 v6, v10, v235 offset0:8 offset1:40
	s_waitcnt vmcnt(3)
	v_add_f32_e32 v11, 1.0, v237
	v_mul_f32_e32 v11, v236, v11
	ds_write2st64_b32 v6, v11, v238 offset0:16 offset1:48
	s_waitcnt vmcnt(0)
	v_add_f32_e32 v8, 1.0, v240
	v_mul_f32_e32 v8, v239, v8
	ds_write2st64_b32 v6, v8, v241 offset0:24 offset1:56
	s_or_b64 exec, exec, s[6:7]
	s_and_saveexec_b64 s[6:7], s[4:5]
	ds_write_b32 v203, v71 offset:55552
	s_or_b64 exec, exec, s[6:7]
	v_ashrrev_i32_e32 v89, 31, v88
	v_lshlrev_b64 v[2:3], 13, v[88:89]
	v_mov_b32_e32 v22, 0
	v_lshl_add_u64 v[18:19], v[86:87], 0, v[2:3]
	s_mov_b32 s6, -4
	v_mov_b64_e32 v[20:21], v[90:91]
	v_mov_b32_e32 v23, v101
	v_mov_b32_e32 v2, 0
	v_mov_b32_e32 v3, v22
	v_mov_b32_e32 v4, v22
	v_mov_b32_e32 v5, v22
	v_mov_b32_e32 v6, v22
	v_mov_b32_e32 v7, v22
	v_mov_b32_e32 v8, v22
	v_mov_b32_e32 v9, v22
	v_mov_b32_e32 v10, v22
	v_mov_b32_e32 v11, v22
	v_mov_b32_e32 v12, v22
	v_mov_b32_e32 v13, v22
	v_mov_b32_e32 v14, v22
	v_mov_b32_e32 v15, v22
	v_mov_b32_e32 v16, v22
	v_mov_b32_e32 v17, v22
	s_waitcnt lgkmcnt(0)
	s_barrier
	global_load_dwordx4 v[230:233], v[18:19], off offset:-48
	global_load_dwordx4 v[234:237], v[18:19], off offset:-32
	global_load_dwordx4 v[238:241], v[18:19], off offset:-16
	global_load_dwordx4 v[242:245], v[18:19], off
	global_load_dword v248, v[20:21], off offset:-1920
	global_load_dword v249, v[20:21], off offset:-1792
	global_load_dword v250, v[20:21], off offset:-1664
	global_load_dword v251, v[20:21], off offset:-1536
	global_load_dword v252, v[20:21], off offset:-1408
	global_load_dword v253, v[20:21], off offset:-1280
	global_load_dword v254, v[20:21], off offset:-1152
	global_load_dword v255, v[20:21], off offset:-1024
	global_load_dword v200, v[20:21], off offset:-896
	global_load_dword v201, v[20:21], off offset:-768
	global_load_dword v202, v[20:21], off offset:-640
	global_load_dword v204, v[20:21], off offset:-512
	global_load_dword v205, v[20:21], off offset:-384
	global_load_dword v109, v[20:21], off offset:-256
	global_load_dword v119, v[20:21], off offset:-128
	global_load_dword v189, v[20:21], off
